# grid barrier poll loops: the s_sleep between polls of the arrival counter removed (back-to-back polls, shorter detection latency)
# baseline (speedup 1.0000x reference)
.LBB0_55:
	global_load_dword v16, v17, s[8:9] sc1
	global_load_dword v1, v17, s[10:11] sc1
	global_load_dword v2, v17, s[20:21] sc1
	global_load_dword v3, v17, s[22:23] sc1
	global_load_dword v4, v17, s[24:25] sc1
	global_load_dword v5, v17, s[26:27] sc1
	global_load_dword v6, v17, s[28:29] sc1
	global_load_dword v7, v17, s[30:31] sc1
	global_load_dword v8, v17, s[34:35] sc1
	global_load_dword v9, v17, s[38:39] sc1
	global_load_dword v10, v17, s[46:47] sc1
	global_load_dword v11, v17, s[48:49] sc1
	global_load_dword v12, v17, s[50:51] sc1
	global_load_dword v13, v17, s[52:53] sc1
	global_load_dword v14, v17, s[54:55] sc1
	global_load_dword v15, v17, s[56:57] sc1
	s_mov_b64 s[58:59], -1
	s_mov_b64 s[60:61], -1
	s_waitcnt vmcnt(14)
	v_add_u32_e32 v18, v1, v16
	s_waitcnt vmcnt(13)
	v_add_u32_e32 v18, v18, v2
	s_waitcnt vmcnt(12)
	v_add_u32_e32 v18, v18, v3
	s_waitcnt vmcnt(11)
	v_add_u32_e32 v18, v18, v4
	s_waitcnt vmcnt(10)
	v_add_u32_e32 v18, v18, v5
	s_waitcnt vmcnt(9)
	v_add_u32_e32 v18, v18, v6
	s_waitcnt vmcnt(8)
	v_add_u32_e32 v18, v18, v7
	s_waitcnt vmcnt(7)
	v_add_u32_e32 v18, v18, v8
	s_waitcnt vmcnt(6)
	v_add_u32_e32 v18, v18, v9
	s_waitcnt vmcnt(5)
	v_add_u32_e32 v18, v18, v10
	s_waitcnt vmcnt(4)
	v_add_u32_e32 v18, v18, v11
	s_waitcnt vmcnt(3)
	v_add_u32_e32 v18, v18, v12
	s_waitcnt vmcnt(2)
	v_add_u32_e32 v18, v18, v13
	s_waitcnt vmcnt(1)
	v_add_u32_e32 v18, v18, v14
	s_waitcnt vmcnt(0)
	v_add_u32_e32 v18, v18, v15
	v_cmp_eq_u32_e32 vcc, s65, v18
	s_cbranch_vccnz .LBB0_54
	s_and_b32 s58, s66, 0xff
	s_cmp_eq_u32 s58, 0
	s_mov_b64 s[58:59], -1
	s_mov_b64 s[62:63], -1
	s_cbranch_scc1 .LBB0_59
	s_and_b64 vcc, exec, s[62:63]
	s_cbranch_vccz .LBB0_54

.LBB0_73:
	s_and_b32 s30, s38, 0xff
	s_mov_b64 s[28:29], -1
	s_cmp_lg_u32 s30, 0
	s_mov_b64 s[34:35], -1
	s_cbranch_scc0 .LBB0_76
	s_and_b64 vcc, exec, s[34:35]
	s_cbranch_vccz .LBB0_72

.LBB0_90:
	s_and_b32 s28, s38, 0xff
	s_cmp_lg_u32 s28, 0
	s_mov_b64 s[30:31], -1
	s_cbranch_scc0 .LBB0_93
	s_mov_b64 s[34:35], -1
	s_and_b64 vcc, exec, s[30:31]
	s_cbranch_vccz .LBB0_89

.LBB0_253:
	global_load_dword v16, v17, s[8:9] sc1
	global_load_dword v1, v17, s[10:11] sc1
	global_load_dword v2, v17, s[12:13] sc1
	global_load_dword v3, v17, s[14:15] sc1
	global_load_dword v4, v17, s[16:17] sc1
	global_load_dword v5, v17, s[18:19] sc1
	global_load_dword v6, v17, s[20:21] sc1
	global_load_dword v7, v17, s[22:23] sc1
	global_load_dword v8, v17, s[24:25] sc1
	global_load_dword v9, v17, s[26:27] sc1
	global_load_dword v10, v17, s[28:29] sc1
	global_load_dword v11, v17, s[30:31] sc1
	global_load_dword v12, v17, s[34:35] sc1
	global_load_dword v13, v17, s[38:39] sc1
	global_load_dword v14, v17, s[46:47] sc1
	global_load_dword v15, v17, s[48:49] sc1
	s_mov_b64 s[50:51], -1
	s_mov_b64 s[52:53], -1
	s_waitcnt vmcnt(14)
	v_add_u32_e32 v18, v1, v16
	s_waitcnt vmcnt(13)
	v_add_u32_e32 v18, v18, v2
	s_waitcnt vmcnt(12)
	v_add_u32_e32 v18, v18, v3
	s_waitcnt vmcnt(11)
	v_add_u32_e32 v18, v18, v4
	s_waitcnt vmcnt(10)
	v_add_u32_e32 v18, v18, v5
	s_waitcnt vmcnt(9)
	v_add_u32_e32 v18, v18, v6
	s_waitcnt vmcnt(8)
	v_add_u32_e32 v18, v18, v7
	s_waitcnt vmcnt(7)
	v_add_u32_e32 v18, v18, v8
	s_waitcnt vmcnt(6)
	v_add_u32_e32 v18, v18, v9
	s_waitcnt vmcnt(5)
	v_add_u32_e32 v18, v18, v10
	s_waitcnt vmcnt(4)
	v_add_u32_e32 v18, v18, v11
	s_waitcnt vmcnt(3)
	v_add_u32_e32 v18, v18, v12
	s_waitcnt vmcnt(2)
	v_add_u32_e32 v18, v18, v13
	s_waitcnt vmcnt(1)
	v_add_u32_e32 v18, v18, v14
	s_waitcnt vmcnt(0)
	v_add_u32_e32 v18, v18, v15
	v_cmp_eq_u32_e32 vcc, s33, v18
	s_cbranch_vccnz .LBB0_252
	s_and_b32 s50, s56, 0xff
	s_cmp_eq_u32 s50, 0
	s_mov_b64 s[50:51], -1
	s_mov_b64 s[54:55], -1
	s_cbranch_scc1 .LBB0_257
	s_and_b64 vcc, exec, s[54:55]
	s_cbranch_vccz .LBB0_252

.LBB0_271:
	s_and_b32 s22, s26, 0xff
	s_mov_b64 s[20:21], -1
	s_cmp_lg_u32 s22, 0
	s_mov_b64 s[24:25], -1
	s_cbranch_scc0 .LBB0_274
	s_and_b64 vcc, exec, s[24:25]
	s_cbranch_vccz .LBB0_270

.LBB0_288:
	s_and_b32 s20, s26, 0xff
	s_cmp_lg_u32 s20, 0
	s_mov_b64 s[22:23], -1
	s_cbranch_scc0 .LBB0_291
	s_mov_b64 s[24:25], -1
	s_and_b64 vcc, exec, s[22:23]
	s_cbranch_vccz .LBB0_287

.LBB0_3492:
	global_load_dword v16, v17, s[8:9] sc1
	global_load_dword v1, v17, s[10:11] sc1
	global_load_dword v2, v17, s[12:13] sc1
	global_load_dword v3, v17, s[14:15] sc1
	global_load_dword v4, v17, s[16:17] sc1
	global_load_dword v5, v17, s[18:19] sc1
	global_load_dword v6, v17, s[20:21] sc1
	global_load_dword v7, v17, s[22:23] sc1
	global_load_dword v8, v17, s[24:25] sc1
	global_load_dword v9, v17, s[26:27] sc1
	global_load_dword v10, v17, s[28:29] sc1
	global_load_dword v11, v17, s[30:31] sc1
	global_load_dword v12, v17, s[34:35] sc1
	global_load_dword v13, v17, s[36:37] sc1
	global_load_dword v14, v17, s[38:39] sc1
	global_load_dword v15, v17, s[46:47] sc1
	s_mov_b64 s[48:49], -1
	s_mov_b64 s[50:51], -1
	s_waitcnt vmcnt(14)
	v_add_u32_e32 v18, v1, v16
	s_waitcnt vmcnt(13)
	v_add_u32_e32 v18, v18, v2
	s_waitcnt vmcnt(12)
	v_add_u32_e32 v18, v18, v3
	s_waitcnt vmcnt(11)
	v_add_u32_e32 v18, v18, v4
	s_waitcnt vmcnt(10)
	v_add_u32_e32 v18, v18, v5
	s_waitcnt vmcnt(9)
	v_add_u32_e32 v18, v18, v6
	s_waitcnt vmcnt(8)
	v_add_u32_e32 v18, v18, v7
	s_waitcnt vmcnt(7)
	v_add_u32_e32 v18, v18, v8
	s_waitcnt vmcnt(6)
	v_add_u32_e32 v18, v18, v9
	s_waitcnt vmcnt(5)
	v_add_u32_e32 v18, v18, v10
	s_waitcnt vmcnt(4)
	v_add_u32_e32 v18, v18, v11
	s_waitcnt vmcnt(3)
	v_add_u32_e32 v18, v18, v12
	s_waitcnt vmcnt(2)
	v_add_u32_e32 v18, v18, v13
	s_waitcnt vmcnt(1)
	v_add_u32_e32 v18, v18, v14
	s_waitcnt vmcnt(0)
	v_add_u32_e32 v18, v18, v15
	v_cmp_eq_u32_e32 vcc, s33, v18
	s_cbranch_vccnz .LBB0_3491
	s_and_b32 s48, s54, 0xff
	s_cmp_eq_u32 s48, 0
	s_mov_b64 s[48:49], -1
	s_mov_b64 s[52:53], -1
	s_cbranch_scc1 .LBB0_3496
	s_and_b64 vcc, exec, s[52:53]
	s_cbranch_vccz .LBB0_3491

.LBB0_3510:
	s_and_b32 s22, s3, 0xff
	s_mov_b64 s[20:21], -1
	s_cmp_lg_u32 s22, 0
	s_mov_b64 s[24:25], -1
	s_cbranch_scc0 .LBB0_3513
	s_and_b64 vcc, exec, s[24:25]
	s_cbranch_vccz .LBB0_3509

.LBB0_3527:
	s_and_b32 s20, s3, 0xff
	s_cmp_lg_u32 s20, 0
	s_mov_b64 s[22:23], -1
	s_cbranch_scc0 .LBB0_3530
	s_mov_b64 s[24:25], -1
	s_and_b64 vcc, exec, s[22:23]
	s_cbranch_vccz .LBB0_3526
